# GDN step 1: log-decay prefix sum on waves 0,1 with DPP row_shr/row_bcast adds instead of six ds_bpermute round trips queued behind the LDS writes
# baseline (speedup 1.0000x reference)
.LBB0_1467:
	v_mov_b32_e32 v61, v3
	v_mov_b32_e32 v0, v68
	s_waitcnt vmcnt(0)
	v_lshrrev_b32_e32 v9, 16, v36
	v_and_b32_e32 v21, 63, v0
	v_mul_u32_u24_e32 v1, 0x88, v21
	v_ashrrev_i32_e32 v60, 3, v0
	v_lshl_add_u32 v1, v1, 1, v61
	v_and_b32_e32 v4, -8, v60
	v_lshl_add_u32 v6, v4, 1, v1
	v_bitop3_b32 v27, v0, 63, v0 bitop3:0xc
	ds_write_b128 v6, v[40:43] offset:18432
	ds_write_b128 v6, v[36:39]
	v_mul_lo_u32 v6, v4, s33
	v_add_u32_e32 v5, 0x16800, v61
	v_add_u32_e32 v7, v61, v6
	v_lshlrev_b32_e32 v11, 1, v21
	v_lshlrev_b32_e32 v13, 1, v27
	v_add_u32_e32 v2, 0x12000, v61
	v_add_u32_e32 v8, v5, v6
	v_add_u32_e32 v12, v7, v11
	v_add_u32_e32 v14, v7, v13
	v_sub_u32_e32 v7, v7, v11
	v_lshrrev_b32_e32 v10, 16, v44
	ds_write_b16 v12, v36 offset:36864
	ds_write_b16 v12, v9 offset:37008
	ds_write_b16 v14, v36 offset:55296
	ds_write_b16 v7, v9 offset:55566
	v_add3_u32 v6, v2, v6, v11
	v_add_u32_e32 v9, v8, v13
	v_sub_u32_e32 v8, v8, v11
	ds_write_b16 v6, v44
	ds_write_b16 v6, v10 offset:144
	ds_write_b16 v9, v44
	ds_write_b16 v8, v10 offset:270
	v_lshrrev_b32_e32 v9, 16, v37
	v_lshrrev_b32_e32 v10, 16, v45
	v_add_u32_e32 v33, 0x200, v0
	ds_write_b16 v12, v37 offset:37152
	ds_write_b16 v12, v9 offset:37296
	ds_write_b16 v7, v37 offset:55710
	ds_write_b16 v7, v9 offset:55854
	ds_write_b16 v6, v45 offset:288
	ds_write_b16 v6, v10 offset:432
	ds_write_b16 v8, v45 offset:414
	ds_write_b16 v8, v10 offset:558
	v_lshrrev_b32_e32 v9, 16, v38
	v_lshrrev_b32_e32 v10, 16, v46
	v_ashrrev_i32_e32 v71, 3, v33
	ds_write_b16 v12, v38 offset:37440
	ds_write_b16 v12, v9 offset:37584
	ds_write_b16 v7, v38 offset:55998
	ds_write_b16 v7, v9 offset:56142
	ds_write_b16 v6, v46 offset:576
	ds_write_b16 v6, v10 offset:720
	ds_write_b16 v8, v46 offset:702
	ds_write_b16 v8, v10 offset:846
	v_lshrrev_b32_e32 v9, 16, v39
	v_lshrrev_b32_e32 v10, 16, v47
	ds_write_b16 v12, v39 offset:37728
	ds_write_b16 v12, v9 offset:37872
	ds_write_b16 v7, v39 offset:56286
	ds_write_b16 v7, v9 offset:56430
	ds_write_b16 v6, v47 offset:864
	ds_write_b16 v6, v10 offset:1008
	ds_write_b16 v8, v47 offset:990
	ds_write_b16 v8, v10 offset:1134
	v_and_b32_e32 v6, -8, v71
	v_lshl_add_u32 v1, v6, 1, v1
	ds_write_b128 v1, v[48:51] offset:18432
	ds_write_b128 v1, v[52:55]
	v_mul_lo_u32 v1, v6, s33
	v_ashrrev_i32_e32 v26, 6, v0
	v_add_u32_e32 v7, v61, v1
	v_add_u32_e32 v5, v5, v1
	v_lshrrev_b32_e32 v8, 16, v52
	v_add_u32_e32 v10, v7, v11
	v_add_u32_e32 v12, v7, v13
	v_sub_u32_e32 v7, v7, v11
	v_add3_u32 v1, v2, v1, v11
	v_add_u32_e32 v2, v5, v13
	v_readfirstlane_b32 s10, v26
	v_lshrrev_b32_e32 v9, 16, v56
	ds_write_b16 v10, v52 offset:36864
	ds_write_b16 v10, v8 offset:37008
	ds_write_b16 v12, v52 offset:55296
	ds_write_b16 v7, v8 offset:55566
	ds_write_b16 v1, v56
	ds_write_b16 v1, v9 offset:144
	ds_write_b16 v2, v56
	v_sub_u32_e32 v2, v5, v11
	v_lshrrev_b32_e32 v5, 16, v53
	v_lshrrev_b32_e32 v8, 16, v57
	s_cmp_lt_i32 s10, 2
	v_lshlrev_b32_e32 v28, 2, v21
	v_add_u32_e32 v22, 0x23400, v61
	ds_write_b16 v2, v9 offset:270
	ds_write_b16 v10, v53 offset:37152
	ds_write_b16 v10, v5 offset:37296
	ds_write_b16 v7, v53 offset:55710
	ds_write_b16 v7, v5 offset:55854
	ds_write_b16 v1, v57 offset:288
	ds_write_b16 v1, v8 offset:432
	ds_write_b16 v2, v57 offset:414
	ds_write_b16 v2, v8 offset:558
	v_lshrrev_b32_e32 v5, 16, v54
	v_lshrrev_b32_e32 v8, 16, v58
	v_add_u32_e32 v23, 0x23200, v61
	s_cselect_b64 s[2:3], -1, 0
	s_cmp_gt_i32 s10, 1
	v_cmp_eq_u32_e32 vcc, 0, v21
	v_lshl_or_b32 v24, s10, 8, v28
	ds_write_b16 v10, v54 offset:37440
	ds_write_b16 v10, v5 offset:37584
	ds_write_b16 v7, v54 offset:55998
	ds_write_b16 v7, v5 offset:56142
	ds_write_b16 v1, v58 offset:576
	ds_write_b16 v1, v8 offset:720
	ds_write_b16 v2, v58 offset:702
	ds_write_b16 v2, v8 offset:846
	v_lshrrev_b32_e32 v5, 16, v55
	v_lshrrev_b32_e32 v8, 16, v59
	ds_write_b16 v10, v55 offset:37728
	ds_write_b16 v10, v5 offset:37872
	ds_write_b16 v7, v55 offset:56286
	ds_write_b16 v7, v5 offset:56430
	ds_write_b16 v1, v59 offset:864
	ds_write_b16 v1, v8 offset:1008
	ds_write_b16 v2, v59 offset:990
	ds_write_b16 v2, v8 offset:1134
	s_cbranch_scc1 .LBB0_1469
	v_mov_b32_e32 v1, v69
	s_nop 1
	v_add_f32_dpp v1, v1, v1 row_shr:1 row_mask:0xf bank_mask:0xf
	s_nop 1
	v_add_f32_dpp v1, v1, v1 row_shr:2 row_mask:0xf bank_mask:0xf
	s_nop 1
	v_add_f32_dpp v1, v1, v1 row_shr:4 row_mask:0xf bank_mask:0xf
	s_nop 1
	v_add_f32_dpp v1, v1, v1 row_shr:8 row_mask:0xf bank_mask:0xf
	s_nop 1
	v_add_f32_dpp v1, v1, v1 row_bcast:15 row_mask:0xa bank_mask:0xf
	s_nop 1
	v_add_f32_dpp v1, v1, v1 row_bcast:31 row_mask:0xc bank_mask:0xf
	s_nop 1
	v_add_u32_e32 v2, v23, v24
	ds_write_b32 v2, v1
	v_add_u32_e32 v1, v22, v24
	ds_write_b32 v1, v70
